# attention softmax fast path: no register copies (exps hoisted), no add-zero; on top of v33
# speedup vs baseline: 1.0074x; 1.0074x over previous
.LBB0_809:
	s_nop 9
	v_exp_f32_e32 v82, v82
	v_exp_f32_e32 v66, v66
	v_exp_f32_e32 v175, v83
	v_exp_f32_e32 v67, v67
	v_exp_f32_e32 v84, v84
	v_exp_f32_e32 v68, v68
	v_exp_f32_e32 v85, v85
	v_exp_f32_e32 v69, v69
	v_add_f32_e32 v83, v66, v82
	v_exp_f32_e32 v86, v86
	v_exp_f32_e32 v70, v70
	v_add_f32_e32 v176, v67, v175
	v_add_f32_e32 v83, v176, v83
	v_add_f32_e32 v176, v68, v84
	v_add_f32_e32 v83, v176, v83
	v_add_f32_e32 v176, v69, v85
	v_add_f32_e32 v83, v176, v83
	v_add_f32_e32 v176, v70, v86
	v_exp_f32_e32 v87, v87
	v_exp_f32_e32 v71, v71
	v_add_f32_e32 v178, v176, v83
	v_exp_f32_e32 v88, v88
	v_exp_f32_e32 v72, v72
	v_add_f32_e32 v179, v71, v87
	v_exp_f32_e32 v176, v89
	v_exp_f32_e32 v83, v73
	v_add_f32_e32 v73, v179, v178
	v_add_f32_e32 v89, v72, v88
	v_add_f32_e32 v178, v89, v73
	v_exp_f32_e32 v89, v90
	v_exp_f32_e32 v73, v74
	v_add_f32_e32 v179, v83, v176
	v_exp_f32_e32 v90, v91
	v_exp_f32_e32 v74, v75
	v_add_f32_e32 v75, v179, v178
	v_add_f32_e32 v91, v73, v89
	v_add_f32_e32 v178, v91, v75
	v_exp_f32_e32 v91, v92
	v_exp_f32_e32 v75, v76
	v_add_f32_e32 v179, v74, v90
	v_exp_f32_e32 v92, v93
	v_exp_f32_e32 v76, v77
	v_add_f32_e32 v77, v179, v178
	v_add_f32_e32 v93, v75, v91
	v_add_f32_e32 v178, v93, v77
	v_exp_f32_e32 v93, v94
	v_exp_f32_e32 v77, v78
	v_add_f32_e32 v179, v76, v92
	v_exp_f32_e32 v94, v95
	v_exp_f32_e32 v78, v79
	v_add_f32_e32 v79, v179, v178
	v_add_f32_e32 v95, v77, v93
	v_add_f32_e32 v79, v95, v79
	v_exp_f32_e32 v95, v96
	v_exp_f32_e32 v80, v80
	v_exp_f32_e32 v96, v97
	v_exp_f32_e32 v81, v81
	v_add_f32_e32 v178, v78, v94
	v_add_f32_e32 v79, v178, v79
	v_add_f32_e32 v97, v80, v95
	v_add_f32_e32 v79, v97, v79
	v_add_f32_e32 v97, v81, v96
	v_add_f32_e32 v79, v97, v79
	v_cmp_ge_f32_e32 vcc, 0x453504f3, v79
	s_cmp_eq_u64 vcc, exec
	s_cbranch_scc0 .Lsm1_slow
	v_mov_b32_e32 v97, 1.0
	s_branch .LBB0_813



.Lsm1_nomask:
	s_nop 7
	v_max_f32_e32 v175, v82, v83


	v_max3_f32 v175, v175, v84, v85
	v_max3_f32 v175, v175, v86, v87
	v_max3_f32 v175, v175, v88, v89
	v_max3_f32 v175, v175, v90, v91
	v_max3_f32 v175, v175, v92, v93
	v_max3_f32 v175, v175, v94, v95
	v_max3_f32 v175, v175, v96, v97
	v_max3_f32 v175, v175, v66, v67
	v_max3_f32 v175, v175, v68, v69
	v_max3_f32 v175, v175, v70, v71
	v_max3_f32 v175, v175, v72, v73
	v_max3_f32 v175, v175, v74, v75
	v_max3_f32 v175, v175, v76, v77
	v_max3_f32 v175, v175, v78, v79
	v_max3_f32 v175, v175, v80, v81
	v_mov_b32_e32 v176, v175
	s_nop 1
	v_permlane32_swap_b32_e32 v175, v176
	v_max_f32_e32 v175, v175, v176
	v_max_f32_e32 v175, 0, v175
	v_sub_f32_e32 v66, v66, v175
	v_sub_f32_e32 v67, v67, v175
	v_sub_f32_e32 v68, v68, v175
	v_sub_f32_e32 v69, v69, v175
	v_sub_f32_e32 v70, v70, v175
	v_sub_f32_e32 v71, v71, v175
	v_sub_f32_e32 v72, v72, v175
	v_sub_f32_e32 v73, v73, v175
	v_sub_f32_e32 v74, v74, v175
	v_sub_f32_e32 v75, v75, v175
	v_sub_f32_e32 v76, v76, v175
	v_sub_f32_e32 v77, v77, v175
	v_sub_f32_e32 v78, v78, v175
	v_sub_f32_e32 v79, v79, v175
	v_sub_f32_e32 v80, v80, v175
	v_sub_f32_e32 v81, v81, v175
	v_sub_f32_e32 v82, v82, v175
	v_sub_f32_e32 v83, v83, v175
	v_sub_f32_e32 v84, v84, v175
	v_sub_f32_e32 v85, v85, v175
	v_sub_f32_e32 v86, v86, v175
	v_sub_f32_e32 v87, v87, v175
	v_sub_f32_e32 v88, v88, v175
	v_sub_f32_e32 v89, v89, v175
	v_sub_f32_e32 v90, v90, v175
	v_sub_f32_e32 v91, v91, v175
	v_sub_f32_e32 v92, v92, v175
	v_sub_f32_e32 v93, v93, v175
	v_sub_f32_e32 v94, v94, v175
	v_sub_f32_e32 v95, v95, v175
	v_sub_f32_e32 v96, v96, v175
	v_sub_f32_e32 v97, v97, v175
	v_exp_f32_e64 v222, -v175
	v_add_f32_e32 v173, v173, v175
	v_sub_f32_e32 v206, 0, v173
	v_mov_b32_e32 v207, v206
	v_mov_b32_e32 v208, v206
	v_mov_b32_e32 v209, v206
	v_mov_b32_e32 v210, v206
	v_mov_b32_e32 v211, v206
	v_mov_b32_e32 v212, v206
	v_mov_b32_e32 v213, v206
	v_mov_b32_e32 v214, v206
	v_mov_b32_e32 v215, v206
	v_mov_b32_e32 v216, v206
	v_mov_b32_e32 v217, v206
	v_mov_b32_e32 v218, v206
	v_mov_b32_e32 v219, v206
	v_mov_b32_e32 v220, v206
	v_mov_b32_e32 v221, v206
	v_exp_f32_e32 v82, v82
	v_exp_f32_e32 v66, v66
	v_exp_f32_e32 v175, v83
	v_exp_f32_e32 v67, v67
	v_exp_f32_e32 v84, v84
	v_exp_f32_e32 v68, v68
	v_exp_f32_e32 v85, v85
	v_exp_f32_e32 v69, v69
	v_add_f32_e32 v83, v66, v82
	v_exp_f32_e32 v86, v86
	v_exp_f32_e32 v70, v70
	v_add_f32_e32 v176, v67, v175
	v_add_f32_e32 v83, v176, v83
	v_add_f32_e32 v176, v68, v84
	v_add_f32_e32 v83, v176, v83
	v_add_f32_e32 v176, v69, v85
	v_add_f32_e32 v83, v176, v83
	v_add_f32_e32 v176, v70, v86
	v_exp_f32_e32 v87, v87
	v_exp_f32_e32 v71, v71
	v_add_f32_e32 v178, v176, v83
	v_exp_f32_e32 v88, v88
	v_exp_f32_e32 v72, v72
	v_add_f32_e32 v179, v71, v87
	v_exp_f32_e32 v176, v89
	v_exp_f32_e32 v83, v73
	v_add_f32_e32 v73, v179, v178
	v_add_f32_e32 v89, v72, v88
	v_add_f32_e32 v178, v89, v73
	v_exp_f32_e32 v89, v90
	v_exp_f32_e32 v73, v74
	v_add_f32_e32 v179, v83, v176
	v_exp_f32_e32 v90, v91
	v_exp_f32_e32 v74, v75
	v_add_f32_e32 v75, v179, v178
	v_add_f32_e32 v91, v73, v89
	v_add_f32_e32 v178, v91, v75
	v_exp_f32_e32 v91, v92
	v_exp_f32_e32 v75, v76
	v_add_f32_e32 v179, v74, v90
	v_exp_f32_e32 v92, v93
	v_exp_f32_e32 v76, v77
	v_add_f32_e32 v77, v179, v178
	v_add_f32_e32 v93, v75, v91
	v_add_f32_e32 v178, v93, v77
	v_exp_f32_e32 v93, v94
	v_exp_f32_e32 v77, v78
	v_add_f32_e32 v179, v76, v92
	v_exp_f32_e32 v94, v95
	v_exp_f32_e32 v78, v79
	v_add_f32_e32 v79, v179, v178
	v_add_f32_e32 v95, v77, v93
	v_add_f32_e32 v79, v95, v79
	v_exp_f32_e32 v95, v96
	v_exp_f32_e32 v80, v80
	v_exp_f32_e32 v96, v97
	v_exp_f32_e32 v81, v81
	v_add_f32_e32 v178, v78, v94
	v_add_f32_e32 v79, v178, v79
	v_add_f32_e32 v97, v80, v95
	v_add_f32_e32 v79, v97, v79
	v_add_f32_e32 v97, v81, v96
	v_add_f32_e32 v79, v97, v79
	v_mov_b32_e32 v97, v222
	v_cmp_gt_f32_e32 vcc, 1.0, v97
	s_branch .Lsm1_join

.LBB0_950:
	s_nop 9
	v_exp_f32_e32 v177, v66
	v_exp_f32_e32 v66, v82
	v_exp_f32_e32 v178, v67
	v_exp_f32_e32 v67, v83
	v_exp_f32_e32 v83, v68
	v_exp_f32_e32 v68, v84
	v_add_f32_e32 v82, v66, v177
	v_add_f32_e32 v179, v67, v178
	v_exp_f32_e32 v84, v69
	v_exp_f32_e32 v69, v85
	v_add_f32_e32 v82, v179, v82
	v_add_f32_e32 v85, v68, v83
	v_add_f32_e32 v82, v85, v82
	v_exp_f32_e32 v85, v70
	v_exp_f32_e32 v70, v86
	v_add_f32_e32 v179, v69, v84
	v_exp_f32_e32 v86, v71
	v_exp_f32_e32 v71, v87
	v_add_f32_e32 v82, v179, v82
	v_add_f32_e32 v87, v70, v85
	v_add_f32_e32 v181, v87, v82
	v_exp_f32_e32 v87, v72
	v_exp_f32_e32 v72, v88
	v_add_f32_e32 v182, v71, v86
	v_exp_f32_e32 v179, v73
	v_exp_f32_e32 v82, v89
	v_add_f32_e32 v73, v182, v181
	v_add_f32_e32 v88, v72, v87
	v_add_f32_e32 v181, v88, v73
	v_exp_f32_e32 v88, v74
	v_exp_f32_e32 v73, v90
	v_add_f32_e32 v182, v82, v179
	v_exp_f32_e32 v89, v75
	v_add_f32_e32 v75, v182, v181
	v_add_f32_e32 v90, v73, v88
	v_add_f32_e32 v181, v90, v75
	v_exp_f32_e32 v74, v91
	v_exp_f32_e32 v90, v76
	v_exp_f32_e32 v75, v92
	v_add_f32_e32 v182, v74, v89
	v_exp_f32_e32 v91, v77
	v_add_f32_e32 v77, v182, v181
	v_add_f32_e32 v92, v75, v90
	v_add_f32_e32 v181, v92, v77
	v_exp_f32_e32 v76, v93
	v_exp_f32_e32 v92, v78
	v_exp_f32_e32 v77, v94
	v_add_f32_e32 v182, v76, v91
	v_exp_f32_e32 v93, v79
	v_add_f32_e32 v79, v182, v181
	v_add_f32_e32 v94, v77, v92
	v_add_f32_e32 v181, v94, v79
	v_exp_f32_e32 v78, v95
	v_exp_f32_e32 v94, v80
	v_exp_f32_e32 v79, v96
	v_exp_f32_e32 v95, v81
	v_exp_f32_e32 v80, v97
	v_add_f32_e32 v182, v78, v93
	v_add_f32_e32 v81, v182, v181
	v_add_f32_e32 v96, v79, v94
	v_add_f32_e32 v81, v96, v81
	v_add_f32_e32 v96, v80, v95
	v_add_f32_e32 v81, v96, v81
	v_cmp_ge_f32_e32 vcc, 0x453504f3, v81
	s_cmp_eq_u64 vcc, exec
	s_cbranch_scc0 .Lsm2_slow
	v_mov_b32_e32 v96, 1.0
	s_branch .LBB0_954



.Lsm2_nomask:
	s_nop 7
	v_max_f32_e32 v177, v66, v67


	v_max3_f32 v177, v177, v68, v69
	v_max3_f32 v177, v177, v70, v71
	v_max3_f32 v177, v177, v72, v73
	v_max3_f32 v177, v177, v74, v75
	v_max3_f32 v177, v177, v76, v77
	v_max3_f32 v177, v177, v78, v79
	v_max3_f32 v177, v177, v80, v81
	v_max3_f32 v177, v177, v82, v83
	v_max3_f32 v177, v177, v84, v85
	v_max3_f32 v177, v177, v86, v87
	v_max3_f32 v177, v177, v88, v89
	v_max3_f32 v177, v177, v90, v91
	v_max3_f32 v177, v177, v92, v93
	v_max3_f32 v177, v177, v94, v95
	v_max3_f32 v177, v177, v96, v97
	v_mov_b32_e32 v178, v177
	s_nop 1
	v_permlane32_swap_b32_e32 v177, v178
	v_max_f32_e32 v177, v177, v178
	v_max_f32_e32 v177, 0, v177
	v_sub_f32_e32 v66, v66, v177
	v_sub_f32_e32 v67, v67, v177
	v_sub_f32_e32 v68, v68, v177
	v_sub_f32_e32 v69, v69, v177
	v_sub_f32_e32 v70, v70, v177
	v_sub_f32_e32 v71, v71, v177
	v_sub_f32_e32 v72, v72, v177
	v_sub_f32_e32 v73, v73, v177
	v_sub_f32_e32 v74, v74, v177
	v_sub_f32_e32 v75, v75, v177
	v_sub_f32_e32 v76, v76, v177
	v_sub_f32_e32 v77, v77, v177
	v_sub_f32_e32 v78, v78, v177
	v_sub_f32_e32 v79, v79, v177
	v_sub_f32_e32 v80, v80, v177
	v_sub_f32_e32 v81, v81, v177
	v_sub_f32_e32 v82, v82, v177
	v_sub_f32_e32 v83, v83, v177
	v_sub_f32_e32 v84, v84, v177
	v_sub_f32_e32 v85, v85, v177
	v_sub_f32_e32 v86, v86, v177
	v_sub_f32_e32 v87, v87, v177
	v_sub_f32_e32 v88, v88, v177
	v_sub_f32_e32 v89, v89, v177
	v_sub_f32_e32 v90, v90, v177
	v_sub_f32_e32 v91, v91, v177
	v_sub_f32_e32 v92, v92, v177
	v_sub_f32_e32 v93, v93, v177
	v_sub_f32_e32 v94, v94, v177
	v_sub_f32_e32 v95, v95, v177
	v_sub_f32_e32 v96, v96, v177
	v_sub_f32_e32 v97, v97, v177
	v_exp_f32_e64 v226, -v177
	v_add_f32_e32 v175, v175, v177
	v_sub_f32_e32 v210, 0, v175
	v_mov_b32_e32 v211, v210
	v_mov_b32_e32 v212, v210
	v_mov_b32_e32 v213, v210
	v_mov_b32_e32 v214, v210
	v_mov_b32_e32 v215, v210
	v_mov_b32_e32 v216, v210
	v_mov_b32_e32 v217, v210
	v_mov_b32_e32 v218, v210
	v_mov_b32_e32 v219, v210
	v_mov_b32_e32 v220, v210
	v_mov_b32_e32 v221, v210
	v_mov_b32_e32 v222, v210
	v_mov_b32_e32 v223, v210
	v_mov_b32_e32 v224, v210
	v_mov_b32_e32 v225, v210
	v_exp_f32_e32 v177, v66
	v_exp_f32_e32 v66, v82
	v_exp_f32_e32 v178, v67
	v_exp_f32_e32 v67, v83
	v_exp_f32_e32 v83, v68
	v_exp_f32_e32 v68, v84
	v_add_f32_e32 v82, v66, v177
	v_add_f32_e32 v179, v67, v178
	v_exp_f32_e32 v84, v69
	v_exp_f32_e32 v69, v85
	v_add_f32_e32 v82, v179, v82
	v_add_f32_e32 v85, v68, v83
	v_add_f32_e32 v82, v85, v82
	v_exp_f32_e32 v85, v70
	v_exp_f32_e32 v70, v86
	v_add_f32_e32 v179, v69, v84
	v_exp_f32_e32 v86, v71
	v_exp_f32_e32 v71, v87
	v_add_f32_e32 v82, v179, v82
	v_add_f32_e32 v87, v70, v85
	v_add_f32_e32 v181, v87, v82
	v_exp_f32_e32 v87, v72
	v_exp_f32_e32 v72, v88
	v_add_f32_e32 v182, v71, v86
	v_exp_f32_e32 v179, v73
	v_exp_f32_e32 v82, v89
	v_add_f32_e32 v73, v182, v181
	v_add_f32_e32 v88, v72, v87
	v_add_f32_e32 v181, v88, v73
	v_exp_f32_e32 v88, v74
	v_exp_f32_e32 v73, v90
	v_add_f32_e32 v182, v82, v179
	v_exp_f32_e32 v89, v75
	v_add_f32_e32 v75, v182, v181
	v_add_f32_e32 v90, v73, v88
	v_add_f32_e32 v181, v90, v75
	v_exp_f32_e32 v74, v91
	v_exp_f32_e32 v90, v76
	v_exp_f32_e32 v75, v92
	v_add_f32_e32 v182, v74, v89
	v_exp_f32_e32 v91, v77
	v_add_f32_e32 v77, v182, v181
	v_add_f32_e32 v92, v75, v90
	v_add_f32_e32 v181, v92, v77
	v_exp_f32_e32 v76, v93
	v_exp_f32_e32 v92, v78
	v_exp_f32_e32 v77, v94
	v_add_f32_e32 v182, v76, v91
	v_exp_f32_e32 v93, v79
	v_add_f32_e32 v79, v182, v181
	v_add_f32_e32 v94, v77, v92
	v_add_f32_e32 v181, v94, v79
	v_exp_f32_e32 v78, v95
	v_exp_f32_e32 v94, v80
	v_exp_f32_e32 v79, v96
	v_exp_f32_e32 v95, v81
	v_exp_f32_e32 v80, v97
	v_add_f32_e32 v182, v78, v93
	v_add_f32_e32 v81, v182, v181
	v_add_f32_e32 v96, v79, v94
	v_add_f32_e32 v81, v96, v81
	v_add_f32_e32 v96, v80, v95
	v_add_f32_e32 v81, v96, v81
	v_mov_b32_e32 v96, v226
	v_cmp_gt_f32_e32 vcc, 1.0, v96
	s_branch .Lsm2_join
